# Layer-1 router phase: router weights staged into LDS with 16 loads in flight per round trip (was 2)
# speedup vs baseline: 1.0228x; 1.0051x over previous
; #define LAS __attribute__((address_space(3)))
; __global__ void __launch_bounds__(NWAVES * 64, 2) trunk_fwd(Args args) {
;     ...
;                 LAS float* RW = (LAS float*)lds;
;                 LAS int* LC = (LAS int*)(lds + 65536);
;                 for (int i = tid; i < 2048 * 8; i += 512) RW[i] = args.in[I_RW][i];
;                 if (tid < 8) LC[tid] = 0;
;                 __syncthreads();
.LBB0_754:
	v_mov_b32_e32 v8, v2
	v_mov_b32_e32 v10, v3
	v_ashrrev_i32_e32 v9, 31, v8
	v_ashrrev_i32_e32 v11, 31, v10
	v_lshl_add_u64 v[8:9], v[8:9], 2, s[40:41]
	v_lshl_add_u64 v[10:11], v[10:11], 2, s[40:41]
	global_load_dword v200, v[8:9], off
	s_nop 0
	global_load_dword v201, v[10:11], off
	s_nop 0
	v_add_u32_e32 v8, 0x400, v2
	v_add_u32_e32 v10, 0x400, v3
	v_ashrrev_i32_e32 v9, 31, v8
	v_ashrrev_i32_e32 v11, 31, v10
	v_lshl_add_u64 v[8:9], v[8:9], 2, s[40:41]
	v_lshl_add_u64 v[10:11], v[10:11], 2, s[40:41]
	global_load_dword v202, v[8:9], off
	s_nop 0
	global_load_dword v203, v[10:11], off
	s_nop 0
	v_add_u32_e32 v8, 0x800, v2
	v_add_u32_e32 v10, 0x800, v3
	v_ashrrev_i32_e32 v9, 31, v8
	v_ashrrev_i32_e32 v11, 31, v10
	v_lshl_add_u64 v[8:9], v[8:9], 2, s[40:41]
	v_lshl_add_u64 v[10:11], v[10:11], 2, s[40:41]
	global_load_dword v204, v[8:9], off
	s_nop 0
	global_load_dword v205, v[10:11], off
	s_nop 0
	v_add_u32_e32 v8, 0xc00, v2
	v_add_u32_e32 v10, 0xc00, v3
	v_ashrrev_i32_e32 v9, 31, v8
	v_ashrrev_i32_e32 v11, 31, v10
	v_lshl_add_u64 v[8:9], v[8:9], 2, s[40:41]
	v_lshl_add_u64 v[10:11], v[10:11], 2, s[40:41]
	global_load_dword v206, v[8:9], off
	s_nop 0
	global_load_dword v207, v[10:11], off
	s_nop 0
	v_add_u32_e32 v8, 0x1000, v2
	v_add_u32_e32 v10, 0x1000, v3
	v_ashrrev_i32_e32 v9, 31, v8
	v_ashrrev_i32_e32 v11, 31, v10
	v_lshl_add_u64 v[8:9], v[8:9], 2, s[40:41]
	v_lshl_add_u64 v[10:11], v[10:11], 2, s[40:41]
	global_load_dword v208, v[8:9], off
	s_nop 0
	global_load_dword v209, v[10:11], off
	s_nop 0
	v_add_u32_e32 v8, 0x1400, v2
	v_add_u32_e32 v10, 0x1400, v3
	v_ashrrev_i32_e32 v9, 31, v8
	v_ashrrev_i32_e32 v11, 31, v10
	v_lshl_add_u64 v[8:9], v[8:9], 2, s[40:41]
	v_lshl_add_u64 v[10:11], v[10:11], 2, s[40:41]
	global_load_dword v210, v[8:9], off
	s_nop 0
	global_load_dword v211, v[10:11], off
	s_nop 0
	v_add_u32_e32 v8, 0x1800, v2
	v_add_u32_e32 v10, 0x1800, v3
	v_ashrrev_i32_e32 v9, 31, v8
	v_ashrrev_i32_e32 v11, 31, v10
	v_lshl_add_u64 v[8:9], v[8:9], 2, s[40:41]
	v_lshl_add_u64 v[10:11], v[10:11], 2, s[40:41]
	global_load_dword v212, v[8:9], off
	s_nop 0
	global_load_dword v213, v[10:11], off
	s_nop 0
	v_add_u32_e32 v8, 0x1c00, v2
	v_add_u32_e32 v10, 0x1c00, v3
	v_ashrrev_i32_e32 v9, 31, v8
	v_ashrrev_i32_e32 v11, 31, v10
	v_lshl_add_u64 v[8:9], v[8:9], 2, s[40:41]
	v_lshl_add_u64 v[10:11], v[10:11], 2, s[40:41]
	global_load_dword v214, v[8:9], off
	s_nop 0
	global_load_dword v215, v[10:11], off
	s_nop 0
	v_add_u32_e32 v6, -8, v6
	s_add_i32 s16, s16, 16
	v_cmp_eq_u32_e32 vcc, 0, v6
	s_or_b64 s[8:9], vcc, s[8:9]
	v_add_u32_e32 v3, 0x2000, v3
	v_add_u32_e32 v2, 0x2000, v2
	s_waitcnt vmcnt(14)
	ds_write2st64_b32 v7, v200, v201 offset1:8
	s_waitcnt vmcnt(12)
	ds_write2st64_b32 v7, v202, v203 offset0:16 offset1:24
	s_waitcnt vmcnt(10)
	ds_write2st64_b32 v7, v204, v205 offset0:32 offset1:40
	s_waitcnt vmcnt(8)
	ds_write2st64_b32 v7, v206, v207 offset0:48 offset1:56
	s_waitcnt vmcnt(6)
	ds_write2st64_b32 v7, v208, v209 offset0:64 offset1:72
	s_waitcnt vmcnt(4)
	ds_write2st64_b32 v7, v210, v211 offset0:80 offset1:88
	s_waitcnt vmcnt(2)
	ds_write2st64_b32 v7, v212, v213 offset0:96 offset1:104
	s_waitcnt vmcnt(0)
	ds_write2st64_b32 v7, v214, v215 offset0:112 offset1:120
	v_add_u32_e32 v7, 0x8000, v7
	v_mov_b32_e32 v8, s16
	s_andn2_b64 exec, exec, s[8:9]
	s_cbranch_execnz .LBB0_754
	s_or_b64 exec, exec, s[8:9]
